# baseline (speedup 1.0000x reference)
_Z8qkv_gemmPKcS0_PKfS2_S2_P14__hip_bfloat16S4_S4_S2_Pc:
	s_cmpk_lt_u32 s2, 0xc0
	s_mov_b64 s[4:5], -1
	s_cbranch_scc0 .LBB1_16
	s_and_b32 s4, s2, 7
	s_mul_i32 s72, s4, 6
	s_lshr_b32 s4, s2, 5
	v_readfirstlane_b32 s3, v0
	s_add_i32 s72, s72, s4
	s_lshr_b32 s73, s72, 4
	s_lshr_b32 s20, s3, 6
	s_cmp_eq_u32 s73, 2
	s_cselect_b64 s[4:5], -1, 0
	s_cmp_lg_u32 s73, 2
	s_cselect_b64 s[24:25], -1, 0
	s_cmpk_lt_u32 s3, 0x200
	s_cselect_b64 s[22:23], -1, 0
	v_and_b32_e32 v34, 63, v0
	v_and_b32_e32 v1, 31, v0
	s_and_b64 vcc, exec, s[22:23]
	s_cbranch_vccz .LBB1_5
	s_load_dwordx4 s[76:79], s[0:1], 0x10
	s_load_dwordx2 s[80:81], s[0:1], 0x20
	s_and_b64 s[6:7], s[4:5], exec
	s_cselect_b32 s6, 0, 0x4000
	s_lshr_b32 s7, s3, 2
	v_lshrrev_b32_e32 v2, 5, v34
	v_and_or_b32 v3, s7, 64, v1
	v_lshlrev_b32_e32 v4, 3, v0
	v_lshrrev_b32_e32 v3, 1, v3
	v_and_or_b32 v2, v4, 8, v2
	v_bitop3_b32 v4, v3, v2, 15 bitop3:0x6c
	v_lshl_or_b32 v3, v3, 8, s6
	s_lshl_b32 s6, s20, 5
	s_and_b32 s6, s6, 0x60
	v_or_b32_e32 v6, s6, v1
	v_lshrrev_b32_e32 v6, 1, v6
	s_and_b64 s[4:5], s[4:5], exec
	v_lshlrev_b32_e32 v4, 4, v4
	v_bitop3_b32 v2, v6, v2, 15 bitop3:0x6c
	s_cselect_b32 s4, 0x4000, 0
	s_waitcnt lgkmcnt(0)
	s_cmp_eq_u32 s73, 1
	s_cselect_b32 s82, s78, s80
	s_cselect_b32 s83, s79, s81
	s_cmp_eq_u32 s73, 0
	s_cselect_b32 s82, s76, s82
	s_cselect_b32 s83, s77, s83
	s_bfe_u32 s84, s2, 0x20003
	s_lshl_b32 s84, s84, 7
	s_cmp_eq_u32 s73, 2
	s_cbranch_scc1 .Lq_bias_v
	s_lshr_b32 s85, s3, 8
	s_lshl_b32 s85, s85, 6
	s_or_b32 s84, s84, s85
	s_lshl_b32 s84, s84, 2
	s_add_u32 s82, s82, s84
	s_addc_u32 s83, s83, 0
	v_lshrrev_b32_e32 v85, 1, v0
	v_and_b32_e32 v85, 16, v85
	global_load_dwordx4 v[100:103], v85, s[82:83]
	global_load_dwordx4 v[104:107], v85, s[82:83] offset:32
	global_load_dwordx4 v[108:111], v85, s[82:83] offset:64
	global_load_dwordx4 v[112:115], v85, s[82:83] offset:96
	global_load_dwordx4 v[116:119], v85, s[82:83] offset:128
	global_load_dwordx4 v[120:123], v85, s[82:83] offset:160
	global_load_dwordx4 v[124:127], v85, s[82:83] offset:192
	global_load_dwordx4 v[128:131], v85, s[82:83] offset:224
	s_branch .Lq_bias_done
.Lq_bias_v:
	s_and_b32 s85, s20, 3
	s_lshl_b32 s85, s85, 5
	s_or_b32 s84, s84, s85
	v_or_b32_e32 v85, s84, v1
	v_lshlrev_b32_e32 v85, 2, v85
	global_load_dword v100, v85, s[82:83]
.Lq_bias_done:
	s_waitcnt lgkmcnt(0)
	s_barrier
	v_or_b32_e32 v35, v3, v4
	v_lshlrev_b32_e32 v2, 4, v2
	v_lshl_or_b32 v6, v6, 8, s4
	v_or_b32_e32 v5, 0x1000, v35
	v_or_b32_e32 v36, v6, v2
	s_movk_i32 s7, 0x60
	s_movk_i32 s4, 0x1020
	v_bitop3_b32 v7, v3, s4, v4 bitop3:0x36
	s_movk_i32 s4, 0x1040
	v_bitop3_b32 v8, v3, s4, v4 bitop3:0x36
	s_movk_i32 s4, 0x1060
	v_bitop3_b32 v37, v3, 32, v4 bitop3:0x36
	v_bitop3_b32 v38, v6, 32, v2 bitop3:0x36
	v_bitop3_b32 v39, v3, 64, v4 bitop3:0x36
	v_bitop3_b32 v40, v6, 64, v2 bitop3:0x36
	v_bitop3_b32 v41, v3, s7, v4 bitop3:0x36
	v_bitop3_b32 v3, v3, s4, v4 bitop3:0x36
	v_bitop3_b32 v42, v6, s7, v2 bitop3:0x36
	v_mov_b32_e32 v18, 0
	s_mov_b32 s4, -4
	v_or_b32_e32 v43, 0x10000, v35
	v_add_u32_e32 v44, 0x10000, v5
	v_or_b32_e32 v45, 0x10000, v36
	v_add_u32_e32 v46, 0x10000, v37
	v_add_u32_e32 v47, 0x10000, v7
	v_add_u32_e32 v48, 0x10000, v38
	v_add_u32_e32 v49, 0x10000, v39
	v_add_u32_e32 v50, 0x10000, v8
	v_add_u32_e32 v51, 0x10000, v40
	v_add_u32_e32 v52, 0x10000, v41
	v_add_u32_e32 v53, 0x10000, v3
	v_add_u32_e32 v54, 0x10000, v42
	v_or_b32_e32 v55, 0x18000, v35
	v_add_u32_e32 v56, 0x18000, v5
	v_or_b32_e32 v57, 0x18000, v36
	v_add_u32_e32 v58, 0x18000, v37
	v_add_u32_e32 v59, 0x18000, v7
	v_add_u32_e32 v60, 0x18000, v38
	v_add_u32_e32 v61, 0x18000, v39
	v_add_u32_e32 v62, 0x18000, v8
	v_add_u32_e32 v63, 0x18000, v40
	v_add_u32_e32 v64, 0x18000, v41
	v_add_u32_e32 v65, 0x18000, v3
	v_add_u32_e32 v66, 0x18000, v42
	v_mov_b32_e32 v19, v18
	v_mov_b32_e32 v20, v18
	v_mov_b32_e32 v21, v18
	v_mov_b32_e32 v22, v18
	v_mov_b32_e32 v23, v18
	v_mov_b32_e32 v24, v18
	v_mov_b32_e32 v25, v18
	v_mov_b32_e32 v26, v18
	v_mov_b32_e32 v27, v18
	v_mov_b32_e32 v28, v18
	v_mov_b32_e32 v29, v18
	v_mov_b32_e32 v30, v18
	v_mov_b32_e32 v31, v18
	v_mov_b32_e32 v32, v18
	v_mov_b32_e32 v33, v18
	v_mov_b32_e32 v2, v18
	v_mov_b32_e32 v3, v18
	v_mov_b32_e32 v4, v18
	v_mov_b32_e32 v5, v18
	v_mov_b32_e32 v6, v18
	v_mov_b32_e32 v7, v18
	v_mov_b32_e32 v8, v18
	v_mov_b32_e32 v9, v18
	v_mov_b32_e32 v10, v18
	v_mov_b32_e32 v11, v18
	v_mov_b32_e32 v12, v18
	v_mov_b32_e32 v13, v18
	v_mov_b32_e32 v14, v18
	v_mov_b32_e32 v15, v18
	v_mov_b32_e32 v16, v18
	v_mov_b32_e32 v17, v18

.LBB1_10:
	s_andn2_b64 vcc, exec, s[22:23]
	s_cbranch_vccnz .LBB1_15
	s_lshr_b32 s16, s3, 8
	s_cmp_eq_u32 s73, 1
	s_waitcnt lgkmcnt(0)
	s_cselect_b32 s10, s10, s12
	s_cselect_b32 s11, s11, s13
	s_cselect_b32 s17, s4, s6
	s_cselect_b32 s18, s5, s7
	s_and_b32 s13, s20, 3
	s_and_b32 s12, s72, 15
	s_cmp_lt_u32 s72, 16
	s_cselect_b64 s[4:5], -1, 0
	s_and_b64 s[6:7], s[4:5], exec
	s_cselect_b32 s9, s9, s11
	s_cselect_b32 s8, s8, s10
	s_cselect_b32 s7, s15, s18
	s_cselect_b32 s6, s14, s17
	s_mov_b64 s[10:11], -1
	s_and_b64 vcc, exec, s[24:25]
	s_cbranch_vccz .LBB1_13
	s_lshl_b32 s10, s74, 7
	s_lshl_b32 s11, s16, 6
	v_lshrrev_b32_e32 v35, 1, v0
	s_or_b32 s14, s11, s10
	v_and_b32_e32 v64, 16, v35
	v_mov_b32_e32 v65, 0
	s_mov_b32 s11, 0
	v_lshl_add_u64 v[36:37], s[8:9], 0, v[64:65]
	s_lshl_b32 s10, s14, 2
	v_lshl_add_u64 v[66:67], v[36:37], 0, s[10:11]
	s_waitcnt vmcnt(0)
	v_mov_b32_e32 v36, v100
	v_mov_b32_e32 v37, v101
	v_mov_b32_e32 v38, v102
	v_mov_b32_e32 v39, v103
	v_mov_b32_e32 v40, v104
	v_mov_b32_e32 v41, v105
	v_mov_b32_e32 v42, v106
	v_mov_b32_e32 v43, v107
	v_mov_b32_e32 v44, v108
	v_mov_b32_e32 v45, v109
	v_mov_b32_e32 v46, v110
	v_mov_b32_e32 v47, v111
	v_mov_b32_e32 v48, v112
	v_mov_b32_e32 v49, v113
	v_mov_b32_e32 v50, v114
	v_mov_b32_e32 v51, v115
	v_mov_b32_e32 v52, v116
	v_mov_b32_e32 v53, v117
	v_mov_b32_e32 v54, v118
	v_mov_b32_e32 v55, v119
	v_mov_b32_e32 v56, v120
	v_mov_b32_e32 v57, v121
	v_mov_b32_e32 v58, v122
	v_mov_b32_e32 v59, v123
	v_mov_b32_e32 v60, v124
	v_mov_b32_e32 v61, v125
	v_mov_b32_e32 v62, v126
	v_mov_b32_e32 v63, v127
	v_mov_b32_e32 v35, 0x3b38aa3b
	v_cndmask_b32_e64 v74, 1.0, v35, s[4:5]
	v_mov_b32_e32 v35, v65
	v_mov_b32_e32 v64, v128
	v_mov_b32_e32 v65, v129
	v_mov_b32_e32 v66, v130
	v_mov_b32_e32 v67, v131
	s_lshl_b32 s10, s12, 2
	s_or_b32 s4, s13, s10
	s_or_b32 s4, s14, s4
	v_lshl_add_u64 v[68:69], s[6:7], 0, v[34:35]
	s_lshl_b32 s14, s4, 2
	s_lshl_b32 s10, s4, 12
	v_lshl_add_u64 v[70:71], v[68:69], 0, s[10:11]
	s_or_b32 s10, s14, 1
	s_lshl_b64 s[4:5], s[10:11], 10
	s_or_b32 s10, s14, 2
	v_lshl_add_u64 v[72:73], v[68:69], 0, s[4:5]
	s_lshl_b64 s[4:5], s[10:11], 10
	s_or_b32 s10, s14, 3
	s_waitcnt vmcnt(0)
	v_add_f32_e32 v35, v18, v36
	v_add_f32_e32 v36, v19, v37
	v_add_f32_e32 v37, v20, v38
	v_add_f32_e32 v38, v21, v39
	v_add_f32_e32 v39, v22, v40
	v_add_f32_e32 v40, v23, v41
	v_add_f32_e32 v41, v24, v42
	v_add_f32_e32 v42, v25, v43
	v_add_f32_e32 v43, v26, v44
	v_mul_f32_e32 v36, v74, v36
	v_mul_f32_e32 v37, v74, v37
	v_mul_f32_e32 v38, v74, v38
	v_mul_f32_e32 v39, v74, v39
	v_add_f32_e32 v44, v27, v45
	v_add_f32_e32 v45, v28, v46
	v_add_f32_e32 v46, v29, v47
	v_add_f32_e32 v47, v30, v48
	v_add_f32_e32 v48, v31, v49
	v_add_f32_e32 v49, v32, v50
	v_add_f32_e32 v50, v33, v51
	v_mul_f32_e32 v35, v74, v35
	v_mul_f32_e32 v40, v74, v40
	v_mul_f32_e32 v41, v74, v41
	v_mul_f32_e32 v42, v74, v42
	v_mul_f32_e32 v43, v74, v43
	v_cvt_pk_bf16_f32 v36, v35, v36
	v_cvt_pk_bf16_f32 v37, v37, v38
	v_cvt_pk_bf16_f32 v38, v39, v40
	v_cvt_pk_bf16_f32 v39, v41, v42
	v_mul_f32_e32 v44, v74, v44
	v_mul_f32_e32 v45, v74, v45
	v_mul_f32_e32 v46, v74, v46
	v_mul_f32_e32 v47, v74, v47
	v_mul_f32_e32 v48, v74, v48
	v_mul_f32_e32 v49, v74, v49
	v_mul_f32_e32 v50, v74, v50
	v_cvt_pk_bf16_f32 v40, v43, v44
	v_cvt_pk_bf16_f32 v41, v45, v46
	v_cvt_pk_bf16_f32 v42, v47, v48
	v_cvt_pk_bf16_f32 v43, v49, v50
	global_store_dwordx4 v[70:71], v[36:39], off
	global_store_dwordx4 v[72:73], v[40:43], off
	v_add_f32_e32 v35, v8, v58
	v_add_f32_e32 v36, v9, v59
	v_mul_f32_e32 v36, v74, v36
	v_add_f32_e32 v51, v2, v52
	v_add_f32_e32 v52, v3, v53
	v_add_f32_e32 v53, v4, v54
	v_add_f32_e32 v54, v5, v55
	v_add_f32_e32 v55, v6, v56
	v_add_f32_e32 v56, v7, v57
	v_mul_f32_e32 v35, v74, v35
	v_cvt_pk_bf16_f32 v47, v35, v36
	v_lshl_add_u64 v[36:37], v[68:69], 0, s[4:5]
	v_mul_f32_e32 v51, v74, v51
	v_mul_f32_e32 v52, v74, v52
	v_mul_f32_e32 v53, v74, v53
	v_mul_f32_e32 v54, v74, v54
	v_mul_f32_e32 v55, v74, v55
	v_mul_f32_e32 v56, v74, v56
	v_cvt_pk_bf16_f32 v44, v51, v52
	v_cvt_pk_bf16_f32 v45, v53, v54
	v_cvt_pk_bf16_f32 v46, v55, v56
	global_store_dwordx4 v[36:37], v[44:47], off
	v_add_f32_e32 v35, v10, v60
	v_add_f32_e32 v36, v11, v61
	v_mul_f32_e32 v35, v74, v35
	v_mul_f32_e32 v36, v74, v36
	v_cvt_pk_bf16_f32 v36, v35, v36
	v_add_f32_e32 v35, v12, v62
	v_add_f32_e32 v37, v13, v63
	v_mul_f32_e32 v35, v74, v35
	v_mul_f32_e32 v37, v74, v37
	v_cvt_pk_bf16_f32 v37, v35, v37
	v_add_f32_e32 v35, v14, v64
	v_add_f32_e32 v38, v15, v65
	v_mul_f32_e32 v35, v74, v35
	v_mul_f32_e32 v38, v74, v38
	v_add_f32_e32 v39, v17, v67
	s_lshl_b64 s[4:5], s[10:11], 10
	v_cvt_pk_bf16_f32 v38, v35, v38
	v_add_f32_e32 v35, v16, v66
	v_mul_f32_e32 v39, v74, v39
	v_lshl_add_u64 v[40:41], v[68:69], 0, s[4:5]
	v_mul_f32_e32 v35, v74, v35
	v_cvt_pk_bf16_f32 v39, v35, v39
	global_store_dwordx4 v[40:41], v[36:39], off
	s_mov_b64 s[10:11], 0
.LBB1_13:
	s_andn2_b64 vcc, exec, s[10:11]
	s_cbranch_vccnz .LBB1_15
	s_lshl_b32 s4, s74, 7
	s_lshl_b32 s5, s13, 5
	s_or_b32 s5, s5, s4
	v_or_b32_e32 v1, s5, v1
	v_lshlrev_b32_e32 v1, 2, v1
	s_waitcnt vmcnt(0)
	v_mov_b32_e32 v1, v100
	s_lshl_b32 s8, s12, 2
	s_lshl_b32 s9, s16, 1
	s_lshl_b32 s10, s20, 5
	v_mov_b32_e32 v35, 0
	s_or_b32 s8, s9, s8
	s_and_b32 s10, s10, 64
	v_lshl_add_u64 v[34:35], s[6:7], 0, v[34:35]
	s_or_b32 s6, s8, s10
	s_or_b32 s4, s6, s4
	s_bfe_u32 s3, s3, 0x10006
	s_lshl_b32 s4, s4, 2
	s_mov_b32 s5, 0
	s_or_b32 s4, s4, s3
	s_mov_b32 s7, s5
	s_mov_b32 s9, s5
	s_lshl_b64 s[10:11], s[4:5], 10
	s_or_b32 s6, s4, 2
	s_or_b32 s8, s4, 4
	s_or_b32 s4, s4, 6
	v_lshl_add_u64 v[36:37], v[34:35], 0, s[10:11]
	s_lshl_b64 s[6:7], s[6:7], 10
	s_lshl_b64 s[8:9], s[8:9], 10
	s_lshl_b64 s[4:5], s[4:5], 10
	v_lshl_add_u64 v[38:39], v[34:35], 0, s[6:7]
	v_lshl_add_u64 v[40:41], v[34:35], 0, s[8:9]
	v_lshl_add_u64 v[34:35], v[34:35], 0, s[4:5]
	s_waitcnt vmcnt(0)
	v_add_f32_e32 v18, v1, v18
	v_add_f32_e32 v19, v1, v19
	v_add_f32_e32 v20, v1, v20
	v_add_f32_e32 v21, v1, v21
	v_add_f32_e32 v22, v1, v22
	v_add_f32_e32 v23, v1, v23
	v_add_f32_e32 v24, v1, v24
	v_add_f32_e32 v25, v1, v25
	v_add_f32_e32 v42, v1, v2
	v_add_f32_e32 v43, v1, v3
	v_add_f32_e32 v44, v1, v4
	v_add_f32_e32 v45, v1, v5
	v_cvt_pk_bf16_f32 v2, v18, v19
	v_cvt_pk_bf16_f32 v3, v20, v21
	v_cvt_pk_bf16_f32 v4, v22, v23
	v_cvt_pk_bf16_f32 v5, v24, v25
	v_add_f32_e32 v26, v1, v26
	v_add_f32_e32 v27, v1, v27
	v_add_f32_e32 v28, v1, v28
	v_add_f32_e32 v29, v1, v29
	v_add_f32_e32 v30, v1, v30
	v_add_f32_e32 v31, v1, v31
	v_add_f32_e32 v32, v1, v32
	v_add_f32_e32 v33, v1, v33
	v_add_f32_e32 v46, v1, v6
	v_add_f32_e32 v47, v1, v7
	v_add_f32_e32 v48, v1, v8
	v_add_f32_e32 v49, v1, v9
	v_add_f32_e32 v50, v1, v10
	v_add_f32_e32 v51, v1, v11
	v_add_f32_e32 v52, v1, v12
	v_add_f32_e32 v53, v1, v13
	v_add_f32_e32 v54, v1, v14
	v_add_f32_e32 v55, v1, v15
	v_add_f32_e32 v56, v1, v16
	v_add_f32_e32 v1, v1, v17
	v_cvt_pk_bf16_f32 v6, v26, v27
	v_cvt_pk_bf16_f32 v7, v28, v29
	v_cvt_pk_bf16_f32 v8, v30, v31
	v_cvt_pk_bf16_f32 v9, v32, v33
	v_cvt_pk_bf16_f32 v10, v42, v43
	v_cvt_pk_bf16_f32 v11, v44, v45
	v_cvt_pk_bf16_f32 v12, v46, v47
	v_cvt_pk_bf16_f32 v13, v48, v49
	v_cvt_pk_bf16_f32 v14, v50, v51
	v_cvt_pk_bf16_f32 v15, v52, v53
	v_cvt_pk_bf16_f32 v16, v54, v55
	v_cvt_pk_bf16_f32 v17, v56, v1
	global_store_dwordx4 v[36:37], v[2:5], off
	global_store_dwordx4 v[38:39], v[6:9], off
	global_store_dwordx4 v[40:41], v[10:13], off
	global_store_dwordx4 v[34:35], v[14:17], off

	.amdhsa_kernel _Z8qkv_gemmPKcS0_PKfS2_S2_P14__hip_bfloat16S4_S4_S2_Pc
		.amdhsa_group_segment_fixed_size 131072
		.amdhsa_private_segment_fixed_size 0
		.amdhsa_kernarg_size 80
		.amdhsa_user_sgpr_count 2
		.amdhsa_user_sgpr_dispatch_ptr 0
		.amdhsa_user_sgpr_queue_ptr 0
		.amdhsa_user_sgpr_kernarg_segment_ptr 1
		.amdhsa_user_sgpr_dispatch_id 0
		.amdhsa_user_sgpr_kernarg_preload_length 0
		.amdhsa_user_sgpr_kernarg_preload_offset 0
		.amdhsa_user_sgpr_private_segment_size 0
		.amdhsa_uses_dynamic_stack 0
		.amdhsa_enable_private_segment 0
		.amdhsa_system_sgpr_workgroup_id_x 1
		.amdhsa_system_sgpr_workgroup_id_y 0
		.amdhsa_system_sgpr_workgroup_id_z 0
		.amdhsa_system_sgpr_workgroup_info 0
		.amdhsa_system_vgpr_workitem_id 0
		.amdhsa_next_free_vgpr 136
		.amdhsa_next_free_sgpr 100
		.amdhsa_accum_offset 136
		.amdhsa_reserve_vcc 1
		.amdhsa_float_round_mode_32 0
		.amdhsa_float_round_mode_16_64 0
		.amdhsa_float_denorm_mode_32 3
		.amdhsa_float_denorm_mode_16_64 3
		.amdhsa_dx10_clamp 1
		.amdhsa_ieee_mode 1
		.amdhsa_fp16_overflow 0
		.amdhsa_tg_split 0
		.amdhsa_exception_fp_ieee_invalid_op 0
		.amdhsa_exception_fp_denorm_src 0
		.amdhsa_exception_fp_ieee_div_zero 0
		.amdhsa_exception_fp_ieee_overflow 0
		.amdhsa_exception_fp_ieee_underflow 0
		.amdhsa_exception_fp_ieee_inexact 0
		.amdhsa_exception_int_div_zero 0
	.end_amdhsa_kernel

amdhsa.kernels:
  - .agpr_count:     0
    .args:
      - .actual_access:  read_only
        .address_space:  global
        .offset:         0
        .size:           8
        .value_kind:     global_buffer
      - .actual_access:  read_only
        .address_space:  global
        .offset:         8
        .size:           8
        .value_kind:     global_buffer
      - .actual_access:  read_only
        .address_space:  global
        .offset:         16
        .size:           8
        .value_kind:     global_buffer
      - .actual_access:  read_only
        .address_space:  global
        .offset:         24
        .size:           8
        .value_kind:     global_buffer
      - .actual_access:  read_only
        .address_space:  global
        .offset:         32
        .size:           8
        .value_kind:     global_buffer
      - .actual_access:  read_only
        .address_space:  global
        .offset:         40
        .size:           8
        .value_kind:     global_buffer
      - .actual_access:  read_only
        .address_space:  global
        .offset:         48
        .size:           8
        .value_kind:     global_buffer
      - .actual_access:  write_only
        .address_space:  global
        .offset:         56
        .size:           8
        .value_kind:     global_buffer
      - .actual_access:  write_only
        .address_space:  global
        .offset:         64
        .size:           8
        .value_kind:     global_buffer
      - .actual_access:  write_only
        .address_space:  global
        .offset:         72
        .size:           8
        .value_kind:     global_buffer
    .group_segment_fixed_size: 0
    .kernarg_segment_align: 8
    .kernarg_segment_size: 80
    .language:       OpenCL C
    .language_version:
      - 2
      - 0
    .max_flat_workgroup_size: 256
    .name:           _Z11prep_kernelPKfS0_S0_S0_S0_S0_S0_PcS1_S1_
    .private_segment_fixed_size: 0
    .sgpr_count:     21
    .sgpr_spill_count: 0
    .symbol:         _Z11prep_kernelPKfS0_S0_S0_S0_S0_S0_PcS1_S1_.kd
    .uniform_work_group_size: 1
    .uses_dynamic_stack: false
    .vgpr_count:     52
    .vgpr_spill_count: 0
    .wavefront_size: 64
  - .agpr_count:     0
    .args:
      - .address_space:  global
        .offset:         0
        .size:           8
        .value_kind:     global_buffer
      - .address_space:  global
        .offset:         8
        .size:           8
        .value_kind:     global_buffer
      - .actual_access:  read_only
        .address_space:  global
        .offset:         16
        .size:           8
        .value_kind:     global_buffer
      - .actual_access:  read_only
        .address_space:  global
        .offset:         24
        .size:           8
        .value_kind:     global_buffer
      - .actual_access:  read_only
        .address_space:  global
        .offset:         32
        .size:           8
        .value_kind:     global_buffer
      - .actual_access:  write_only
        .address_space:  global
        .offset:         40
        .size:           8
        .value_kind:     global_buffer
      - .actual_access:  write_only
        .address_space:  global
        .offset:         48
        .size:           8
        .value_kind:     global_buffer
      - .actual_access:  write_only
        .address_space:  global
        .offset:         56
        .size:           8
        .value_kind:     global_buffer
      - .actual_access:  read_only
        .address_space:  global
        .offset:         64
        .size:           8
        .value_kind:     global_buffer
      - .actual_access:  write_only
        .address_space:  global
        .offset:         72
        .size:           8
        .value_kind:     global_buffer
    .group_segment_fixed_size: 131072
    .kernarg_segment_align: 8
    .kernarg_segment_size: 80
    .language:       OpenCL C
    .language_version:
      - 2
      - 0
    .max_flat_workgroup_size: 768
    .name:           _Z8qkv_gemmPKcS0_PKfS2_S2_P14__hip_bfloat16S4_S4_S2_Pc
    .private_segment_fixed_size: 0
    .sgpr_count:     106
    .sgpr_spill_count: 2
    .symbol:         _Z8qkv_gemmPKcS0_PKfS2_S2_P14__hip_bfloat16S4_S4_S2_Pc.kd
    .uniform_work_group_size: 1
    .uses_dynamic_stack: false
    .vgpr_count:     136
    .vgpr_spill_count: 0
    .wavefront_size: 64
  - .agpr_count:     0
    .args:
      - .address_space:  global
        .offset:         0
        .size:           8
        .value_kind:     global_buffer
      - .address_space:  global
        .offset:         8
        .size:           8
        .value_kind:     global_buffer
      - .address_space:  global
        .offset:         16
        .size:           8
        .value_kind:     global_buffer
      - .actual_access:  write_only
        .address_space:  global
        .offset:         24
        .size:           8
        .value_kind:     global_buffer
    .group_segment_fixed_size: 35840
    .kernarg_segment_align: 8
    .kernarg_segment_size: 32
    .language:       OpenCL C
    .language_version:
      - 2
      - 0
    .max_flat_workgroup_size: 256
    .name:           _Z11attn_kernelPK14__hip_bfloat16S1_S1_PS_
    .private_segment_fixed_size: 0
    .sgpr_count:     84
    .sgpr_spill_count: 0
    .symbol:         _Z11attn_kernelPK14__hip_bfloat16S1_S1_PS_.kd
    .uniform_work_group_size: 1
    .uses_dynamic_stack: false
    .vgpr_count:     204
    .vgpr_spill_count: 0
    .wavefront_size: 64
  - .agpr_count:     0
    .args:
      - .address_space:  global
        .offset:         0
        .size:           8
        .value_kind:     global_buffer
      - .address_space:  global
        .offset:         8
        .size:           8
        .value_kind:     global_buffer
      - .actual_access:  read_only
        .address_space:  global
        .offset:         16
        .size:           8
        .value_kind:     global_buffer
      - .actual_access:  read_only
        .address_space:  global
        .offset:         24
        .size:           8
        .value_kind:     global_buffer
      - .actual_access:  write_only
        .address_space:  global
        .offset:         32
        .size:           8
        .value_kind:     global_buffer
    .group_segment_fixed_size: 147456
    .kernarg_segment_align: 8
    .kernarg_segment_size: 40
    .language:       OpenCL C
    .language_version:
      - 2
      - 0
    .max_flat_workgroup_size: 512
    .name:           _Z7fc_gemmPKcS0_PKfS2_Pf
    .private_segment_fixed_size: 0
    .sgpr_count:     21
    .sgpr_spill_count: 0
    .symbol:         _Z7fc_gemmPKcS0_PKfS2_Pf.kd
    .uniform_work_group_size: 1
    .uses_dynamic_stack: false
    .vgpr_count:     192
    .vgpr_spill_count: 0
    .wavefront_size: 64
  - .agpr_count:     0
    .args:
      - .actual_access:  read_only
        .address_space:  global
        .offset:         0
        .size:           8
        .value_kind:     global_buffer
      - .actual_access:  write_only
        .address_space:  global
        .offset:         8
        .size:           8
        .value_kind:     global_buffer
      - .actual_access:  read_only
        .address_space:  global
        .offset:         16
        .size:           8
        .value_kind:     global_buffer
      - .actual_access:  read_only
        .address_space:  global
        .offset:         24
        .size:           8
        .value_kind:     global_buffer
    .group_segment_fixed_size: 16
    .kernarg_segment_align: 8
    .kernarg_segment_size: 32
    .language:       OpenCL C
    .language_version:
      - 2
      - 0
    .max_flat_workgroup_size: 256
    .name:           _Z9ln_kernelPKfPfS0_S0_
    .private_segment_fixed_size: 0
    .sgpr_count:     18
    .sgpr_spill_count: 0
    .symbol:         _Z9ln_kernelPKfPfS0_S0_.kd
    .uniform_work_group_size: 1
    .uses_dynamic_stack: false
    .vgpr_count:     74
    .vgpr_spill_count: 0
    .wavefront_size: 64
  - .agpr_count:     0
    .args:           []
    .group_segment_fixed_size: 0
    .kernarg_segment_align: 4
    .kernarg_segment_size: 0
    .language:       OpenCL C
    .language_version:
      - 2
      - 0
    .max_flat_workgroup_size: 1024
    .name:           _Z12empty_kernelv
    .private_segment_fixed_size: 0
    .sgpr_count:     6
    .sgpr_spill_count: 0
    .symbol:         _Z12empty_kernelv.kd
    .uniform_work_group_size: 1
    .uses_dynamic_stack: false
    .vgpr_count:     0
    .vgpr_spill_count: 0
    .wavefront_size: 64
